# baseline (speedup 1.0000x reference)
.LBB0_3:
	s_or_b64 exec, exec, s[2:3]
	s_mov_b32 s0, 0x8000
	v_cmp_gt_i32_e32 vcc, s0, v2
	v_ashrrev_i32_e32 v3, 31, v2
	s_and_saveexec_b64 s[0:1], vcc
	s_cbranch_execz .LBB0_5
	v_lshl_add_u64 v[4:5], v[2:3], 2, s[12:13]
	global_load_dword v66, v[4:5], off
.LBB0_5:
	s_or_b64 exec, exec, s[0:1]
	s_movk_i32 s0, 0x4000
	v_cmp_gt_i32_e32 vcc, s0, v2
	s_and_saveexec_b64 s[0:1], vcc
	s_cbranch_execz .LBB0_7
	v_lshl_add_u64 v[4:5], v[2:3], 2, s[18:19]
	global_load_dword v67, v[4:5], off
.LBB0_7:
	s_or_b64 exec, exec, s[0:1]
	s_movk_i32 s0, 0x400
	v_cmp_gt_i32_e32 vcc, s0, v2
	s_and_saveexec_b64 s[0:1], vcc
	s_cbranch_execz .Lpw_tail
	v_ashrrev_i32_e32 v1, 7, v2
	v_cmp_gt_i32_e32 vcc, 4, v1
	v_lshlrev_b32_e32 v1, 6, v1
	v_mov_b32_e32 v5, s17
	v_mov_b32_e32 v6, s15
	v_and_b32_e32 v1, 0xc0, v1
	v_and_b32_e32 v4, 0x7f, v0
	v_cndmask_b32_e32 v7, v5, v6, vcc
	v_mov_b32_e32 v5, s16
	v_mov_b32_e32 v6, s14
	v_lshlrev_b32_e32 v40, 9, v1
	v_cndmask_b32_e32 v6, v5, v6, vcc
	v_lshl_or_b32 v41, v4, 2, v40
	v_lshlrev_b32_e32 v4, 2, v1
	v_mov_b32_e32 v5, 0
	v_lshl_add_u64 v[6:7], v[6:7], 0, v[4:5]
	global_load_dword v32, v41, s[12:13]
	global_load_dwordx4 v[8:11], v[6:7], off
	v_or_b32_e32 v1, 0x200, v41
	v_or_b32_e32 v4, 0x400, v41
	v_or_b32_e32 v16, 0x600, v41
	global_load_dword v33, v1, s[12:13]
	global_load_dword v34, v4, s[12:13]
	global_load_dword v35, v16, s[12:13]
	global_load_dwordx4 v[12:15], v[6:7], off offset:16
	v_or_b32_e32 v1, 0x800, v41
	global_load_dword v1, v1, s[12:13]
	v_or_b32_e32 v4, 0xa00, v41
	global_load_dword v4, v4, s[12:13]
	v_or_b32_e32 v16, 0xc00, v41
	global_load_dword v36, v16, s[12:13]
	v_or_b32_e32 v20, 0xe00, v41
	global_load_dword v37, v20, s[12:13]
	global_load_dwordx4 v[16:19], v[6:7], off offset:32
	v_or_b32_e32 v20, 0x1000, v41
	global_load_dword v38, v20, s[12:13]
	v_or_b32_e32 v20, 0x1200, v41
	v_or_b32_e32 v21, 0x1400, v41
	global_load_dword v39, v20, s[12:13]
	global_load_dword v42, v21, s[12:13]
	v_or_b32_e32 v24, 0x1600, v41
	global_load_dword v43, v24, s[12:13]
	global_load_dwordx4 v[20:23], v[6:7], off offset:48
	v_or_b32_e32 v24, 0x1800, v41
	v_or_b32_e32 v25, 0x1a00, v41
	global_load_dword v44, v24, s[12:13]
	global_load_dword v45, v25, s[12:13]
	v_or_b32_e32 v24, 0x1c00, v41
	global_load_dword v46, v24, s[12:13]
	v_or_b32_e32 v28, 0x1e00, v41
	global_load_dwordx4 v[24:27], v[6:7], off offset:64
	v_or_b32_e32 v29, 0x2000, v41
	v_or_b32_e32 v30, 0x2200, v41
	v_or_b32_e32 v31, 0x2400, v41
	global_load_dword v47, v28, s[12:13]
	global_load_dword v48, v29, s[12:13]
	global_load_dword v49, v30, s[12:13]
	global_load_dword v50, v31, s[12:13]
	v_or_b32_e32 v51, 0x2600, v41
	global_load_dword v52, v51, s[12:13]
	global_load_dwordx4 v[28:31], v[6:7], off offset:80
	v_or_b32_e32 v51, 0x2800, v41
	v_or_b32_e32 v53, 0x2a00, v41
	v_or_b32_e32 v54, 0x2c00, v41
	v_or_b32_e32 v55, 0x2e00, v41
	global_load_dword v56, v51, s[12:13]
	global_load_dword v57, v53, s[12:13]
	global_load_dword v58, v54, s[12:13]
	global_load_dword v59, v55, s[12:13]
	v_or_b32_e32 v53, 0x3000, v41
	v_or_b32_e32 v54, 0x3200, v41
	v_lshlrev_b32_e32 v0, 2, v0
	s_movk_i32 s0, 0x7e00
	v_or3_b32 v0, v40, v0, s0
	s_waitcnt vmcnt(28)
	v_cvt_f16_f32_e32 v66, v66
	v_lshl_add_u64 v[70:71], v[2:3], 1, s[8:9]
	global_store_short v[70:71], v66, off
	v_cvt_f16_f32_e32 v67, v67
	v_lshl_add_u64 v[68:69], v[2:3], 1, s[10:11]
	global_store_short v[68:69], v67, off
	v_fma_f32 v51, v32, v8, 0
	s_waitcnt vmcnt(27)
	v_fmac_f32_e32 v51, v33, v9
	s_waitcnt vmcnt(26)
	v_fmac_f32_e32 v51, v34, v10
	s_waitcnt vmcnt(25)
	v_fmac_f32_e32 v51, v35, v11
	global_load_dwordx4 v[8:11], v[6:7], off offset:112
	global_load_dwordx4 v[32:35], v[6:7], off offset:96
	s_waitcnt vmcnt(25)
	v_fmac_f32_e32 v51, v1, v12
	v_or_b32_e32 v1, 0x3400, v41
	s_waitcnt vmcnt(24)
	v_fmac_f32_e32 v51, v4, v13
	v_or_b32_e32 v4, 0x3600, v41
	global_load_dword v55, v53, s[12:13]
	global_load_dword v60, v54, s[12:13]
	global_load_dword v61, v1, s[12:13]
	global_load_dword v62, v4, s[12:13]
	v_or_b32_e32 v12, 0x3800, v41
	s_waitcnt vmcnt(27)
	v_fmac_f32_e32 v51, v36, v14
	v_or_b32_e32 v13, 0x3a00, v41
	v_or_b32_e32 v14, 0x3c00, v41
	v_or_b32_e32 v1, 0x3e00, v41
	v_or_b32_e32 v4, 0x4000, v41
	global_load_dword v53, v12, s[12:13]
	global_load_dword v54, v13, s[12:13]
	global_load_dword v63, v14, s[12:13]
	global_load_dword v64, v1, s[12:13]
	global_load_dword v65, v4, s[12:13]
	s_waitcnt vmcnt(31)
	v_fmac_f32_e32 v51, v37, v15
	global_load_dwordx4 v[12:15], v[6:7], off offset:128
	v_or_b32_e32 v1, 0x4200, v41
	s_waitcnt vmcnt(30)
	v_fmac_f32_e32 v51, v38, v16
	global_load_dword v1, v1, s[12:13]
	v_or_b32_e32 v4, 0x4400, v41
	s_waitcnt vmcnt(30)
	v_fmac_f32_e32 v51, v39, v17
	global_load_dword v4, v4, s[12:13]
	v_or_b32_e32 v16, 0x4600, v41
	s_waitcnt vmcnt(30)
	v_fmac_f32_e32 v51, v42, v18
	global_load_dword v42, v16, s[12:13]
	s_waitcnt vmcnt(30)
	v_fmac_f32_e32 v51, v43, v19
	s_waitcnt vmcnt(28)
	v_fmac_f32_e32 v51, v44, v20
	v_or_b32_e32 v20, 0x4800, v41
	global_load_dword v43, v20, s[12:13]
	global_load_dwordx4 v[16:19], v[6:7], off offset:144
	s_waitcnt vmcnt(29)
	v_fmac_f32_e32 v51, v45, v21
	s_waitcnt vmcnt(28)
	v_fmac_f32_e32 v51, v46, v22
	s_waitcnt vmcnt(26)
	v_fmac_f32_e32 v51, v47, v23
	s_waitcnt vmcnt(25)
	v_fmac_f32_e32 v51, v48, v24
	s_waitcnt vmcnt(24)
	v_fmac_f32_e32 v51, v49, v25
	s_waitcnt vmcnt(23)
	v_fmac_f32_e32 v51, v50, v26
	s_waitcnt vmcnt(22)
	v_fmac_f32_e32 v51, v52, v27
	s_waitcnt vmcnt(20)
	v_fmac_f32_e32 v51, v56, v28
	s_waitcnt vmcnt(19)
	v_fmac_f32_e32 v51, v57, v29
	v_or_b32_e32 v24, 0x4a00, v41
	s_waitcnt vmcnt(18)
	v_fmac_f32_e32 v51, v58, v30
	global_load_dwordx4 v[20:23], v[6:7], off offset:176
	global_load_dwordx4 v[36:39], v[6:7], off offset:160
	v_or_b32_e32 v25, 0x4c00, v41
	v_or_b32_e32 v26, 0x4e00, v41
	v_or_b32_e32 v27, 0x5000, v41
	global_load_dword v44, v24, s[12:13]
	global_load_dword v45, v25, s[12:13]
	global_load_dword v46, v26, s[12:13]
	global_load_dword v47, v27, s[12:13]
	s_waitcnt vmcnt(23)
	v_fmac_f32_e32 v51, v59, v31
	v_or_b32_e32 v24, 0x5200, v41
	v_or_b32_e32 v25, 0x5400, v41
	v_or_b32_e32 v26, 0x5600, v41
	v_or_b32_e32 v27, 0x5800, v41
	v_or_b32_e32 v28, 0x5a00, v41
	v_or_b32_e32 v29, 0x5c00, v41
	v_or_b32_e32 v30, 0x5e00, v41
	v_or_b32_e32 v31, 0x6000, v41
	global_load_dword v48, v24, s[12:13]
	global_load_dword v49, v25, s[12:13]
	global_load_dword v50, v26, s[12:13]
	global_load_dword v52, v27, s[12:13]
	global_load_dword v56, v28, s[12:13]
	global_load_dword v57, v29, s[12:13]
	global_load_dword v58, v30, s[12:13]
	global_load_dword v59, v31, s[12:13]
	s_nop 0
	global_load_dwordx4 v[24:27], v[6:7], off offset:240
	global_load_dwordx4 v[28:31], v[6:7], off offset:224
	s_waitcnt vmcnt(30)
	v_fmac_f32_e32 v51, v55, v32
	s_waitcnt vmcnt(29)
	v_fmac_f32_e32 v51, v60, v33
	s_waitcnt vmcnt(28)
	v_fmac_f32_e32 v51, v61, v34
	s_waitcnt vmcnt(27)
	v_fmac_f32_e32 v51, v62, v35
	s_waitcnt vmcnt(26)
	v_fmac_f32_e32 v51, v53, v8
	s_waitcnt vmcnt(25)
	v_fmac_f32_e32 v51, v54, v9
	s_waitcnt vmcnt(24)
	v_fmac_f32_e32 v51, v63, v10
	s_waitcnt vmcnt(23)
	v_fmac_f32_e32 v51, v64, v11
	global_load_dwordx4 v[8:11], v[6:7], off offset:208
	global_load_dwordx4 v[32:35], v[6:7], off offset:192
	v_or_b32_e32 v6, 0x6200, v41
	s_waitcnt vmcnt(23)
	v_fmac_f32_e32 v51, v65, v12
	v_or_b32_e32 v7, 0x6400, v41
	v_or_b32_e32 v53, 0x6600, v41
	s_waitcnt vmcnt(22)
	v_fmac_f32_e32 v51, v1, v13
	v_or_b32_e32 v12, 0x6800, v41
	v_or_b32_e32 v1, 0x6a00, v41
	s_waitcnt vmcnt(21)
	v_fmac_f32_e32 v51, v4, v14
	v_or_b32_e32 v4, 0x6c00, v41
	v_or_b32_e32 v13, 0x6e00, v41
	s_waitcnt vmcnt(20)
	v_fmac_f32_e32 v51, v42, v15
	v_or_b32_e32 v14, 0x7000, v41
	global_load_dword v15, v6, s[12:13]
	global_load_dword v42, v7, s[12:13]
	global_load_dword v54, v53, s[12:13]
	global_load_dword v55, v12, s[12:13]
	global_load_dword v60, v1, s[12:13]
	global_load_dword v61, v4, s[12:13]
	global_load_dword v62, v13, s[12:13]
	global_load_dword v63, v14, s[12:13]
	v_or_b32_e32 v1, 0x7200, v41
	v_or_b32_e32 v4, 0x7400, v41
	v_or_b32_e32 v6, 0x7600, v41
	v_or_b32_e32 v7, 0x7800, v41
	s_waitcnt vmcnt(26)
	v_fmac_f32_e32 v51, v43, v16
	v_or_b32_e32 v12, 0x7a00, v41
	v_or_b32_e32 v13, 0x7c00, v41
	global_load_dword v14, v1, s[12:13]
	global_load_dword v16, v4, s[12:13]
	global_load_dword v40, v6, s[12:13]
	global_load_dword v41, v7, s[12:13]
	global_load_dword v43, v12, s[12:13]
	global_load_dword v53, v13, s[12:13]
	global_load_dword v64, v0, s[12:13]
	v_lshl_add_u64 v[0:1], v[2:3], 2, s[4:5]
	s_waitcnt vmcnt(30)
	v_fmac_f32_e32 v51, v44, v17
	s_waitcnt vmcnt(29)
	v_fmac_f32_e32 v51, v45, v18
	s_waitcnt vmcnt(28)
	v_fmac_f32_e32 v51, v46, v19
	s_waitcnt vmcnt(27)
	v_fmac_f32_e32 v51, v47, v36
	s_waitcnt vmcnt(26)
	v_fmac_f32_e32 v51, v48, v37
	s_waitcnt vmcnt(25)
	v_fmac_f32_e32 v51, v49, v38
	s_waitcnt vmcnt(24)
	v_fmac_f32_e32 v51, v50, v39
	s_waitcnt vmcnt(23)
	v_fmac_f32_e32 v51, v52, v20
	s_waitcnt vmcnt(22)
	v_fmac_f32_e32 v51, v56, v21
	s_waitcnt vmcnt(21)
	v_fmac_f32_e32 v51, v57, v22
	s_waitcnt vmcnt(20)
	v_fmac_f32_e32 v51, v58, v23
	s_waitcnt vmcnt(15)
	v_fmac_f32_e32 v51, v59, v32
	s_waitcnt vmcnt(14)
	v_fmac_f32_e32 v51, v15, v33
	s_waitcnt vmcnt(13)
	v_fmac_f32_e32 v51, v42, v34
	s_waitcnt vmcnt(12)
	v_fmac_f32_e32 v51, v54, v35
	s_waitcnt vmcnt(11)
	v_fmac_f32_e32 v51, v55, v8
	s_waitcnt vmcnt(10)
	v_fmac_f32_e32 v51, v60, v9
	s_waitcnt vmcnt(9)
	v_fmac_f32_e32 v51, v61, v10
	s_waitcnt vmcnt(8)
	v_fmac_f32_e32 v51, v62, v11
	s_waitcnt vmcnt(7)
	v_fmac_f32_e32 v51, v63, v28
	s_waitcnt vmcnt(6)
	v_fmac_f32_e32 v51, v14, v29
	s_waitcnt vmcnt(5)
	v_fmac_f32_e32 v51, v16, v30
	s_waitcnt vmcnt(4)
	v_fmac_f32_e32 v51, v40, v31
	s_waitcnt vmcnt(3)
	v_fmac_f32_e32 v51, v41, v24
	s_waitcnt vmcnt(2)
	v_fmac_f32_e32 v51, v43, v25
	s_waitcnt vmcnt(1)
	v_fmac_f32_e32 v51, v53, v26
	s_waitcnt vmcnt(0)
	v_fma_mixlo_f16 v6, v64, v27, v51
	v_cvt_f32_f16_e32 v7, v6
	v_fma_f32 v4, v64, v27, v51
	global_store_dword v[0:1], v4, off
	v_lshl_add_u64 v[0:1], v[2:3], 1, s[6:7]
	v_sub_f32_e32 v2, v4, v7
	v_cvt_f16_f32_e32 v4, v2
	v_add_co_u32_e32 v2, vcc, 0x1000, v0
	global_store_short v[0:1], v6, off
	s_nop 0
	v_addc_co_u32_e32 v3, vcc, 0, v1, vcc
	global_store_short v[2:3], v4, off
	global_store_short v[0:1], v5, off offset:2048
	global_store_short v[2:3], v5, off offset:2048

.Lpw_tail:
	s_or_b64 exec, exec, s[0:1]
	s_waitcnt vmcnt(0)
	s_mov_b32 s0, 0x8000
	v_cmp_gt_i32_e32 vcc, s0, v2
	s_and_saveexec_b64 s[0:1], vcc
	v_cvt_f16_f32_e32 v66, v66
	v_lshl_add_u64 v[4:5], v[2:3], 1, s[8:9]
	global_store_short v[4:5], v66, off
	s_movk_i32 s2, 0x4000
	v_cmp_gt_i32_e32 vcc, s2, v2
	s_and_b64 exec, exec, vcc
	v_cvt_f16_f32_e32 v67, v67
	v_lshl_add_u64 v[4:5], v[2:3], 1, s[10:11]
	global_store_short v[4:5], v67, off
	s_endpgm

	.amdhsa_kernel _Z7k_prepwPKfS0_S0_S0_PfPDF16_S2_S2_Pii
		.amdhsa_group_segment_fixed_size 0
		.amdhsa_private_segment_fixed_size 0
		.amdhsa_kernarg_size 336
		.amdhsa_user_sgpr_count 2
		.amdhsa_user_sgpr_dispatch_ptr 0
		.amdhsa_user_sgpr_queue_ptr 0
		.amdhsa_user_sgpr_kernarg_segment_ptr 1
		.amdhsa_user_sgpr_dispatch_id 0
		.amdhsa_user_sgpr_kernarg_preload_length 0
		.amdhsa_user_sgpr_kernarg_preload_offset 0
		.amdhsa_user_sgpr_private_segment_size 0
		.amdhsa_uses_dynamic_stack 0
		.amdhsa_enable_private_segment 0
		.amdhsa_system_sgpr_workgroup_id_x 1
		.amdhsa_system_sgpr_workgroup_id_y 0
		.amdhsa_system_sgpr_workgroup_id_z 0
		.amdhsa_system_sgpr_workgroup_info 0
		.amdhsa_system_vgpr_workitem_id 0
		.amdhsa_next_free_vgpr 72
		.amdhsa_next_free_sgpr 24
		.amdhsa_accum_offset 72
		.amdhsa_reserve_vcc 1
		.amdhsa_float_round_mode_32 0
		.amdhsa_float_round_mode_16_64 0
		.amdhsa_float_denorm_mode_32 3
		.amdhsa_float_denorm_mode_16_64 3
		.amdhsa_dx10_clamp 1
		.amdhsa_ieee_mode 1
		.amdhsa_fp16_overflow 0
		.amdhsa_tg_split 0
		.amdhsa_exception_fp_ieee_invalid_op 0
		.amdhsa_exception_fp_denorm_src 0
		.amdhsa_exception_fp_ieee_div_zero 0
		.amdhsa_exception_fp_ieee_overflow 0
		.amdhsa_exception_fp_ieee_underflow 0
		.amdhsa_exception_fp_ieee_inexact 0
		.amdhsa_exception_int_div_zero 0
	.end_amdhsa_kernel

_Z7k_finalPKfPKiS0_S0_Pf:
	s_load_dwordx2 s[2:3], s[0:1], 0x0
	s_load_dwordx8 s[12:19], s[0:1], 0x0
	s_load_dwordx2 s[20:21], s[0:1], 0x20
	v_mov_b32_e32 v3, 0
	v_lshlrev_b32_e32 v2, 2, v0
	v_mov_b32_e32 v11, 0
	s_waitcnt lgkmcnt(0)
	v_lshl_add_u64 v[4:5], s[2:3], 0, v[2:3]
	v_add_co_u32_e32 v12, vcc, 0x1000, v4
	s_nop 1
	v_addc_co_u32_e32 v13, vcc, 0, v5, vcc
	v_add_co_u32_e32 v14, vcc, 0x2000, v4
	s_nop 1
	v_addc_co_u32_e32 v15, vcc, 0, v5, vcc
	v_add_co_u32_e32 v16, vcc, 0x3000, v4
	s_nop 1
	v_addc_co_u32_e32 v17, vcc, 0, v5, vcc
	v_add_co_u32_e32 v18, vcc, 0x4000, v4
	s_nop 1
	v_addc_co_u32_e32 v19, vcc, 0, v5, vcc
	v_add_co_u32_e32 v20, vcc, 0x5000, v4
	s_nop 1
	v_addc_co_u32_e32 v21, vcc, 0, v5, vcc
	v_add_co_u32_e32 v22, vcc, 0x6000, v4
	s_nop 1
	v_addc_co_u32_e32 v23, vcc, 0, v5, vcc
	v_add_co_u32_e32 v24, vcc, 0x7000, v4
	s_nop 1
	v_addc_co_u32_e32 v25, vcc, 0, v5, vcc
	global_load_dword v1, v2, s[2:3]
	global_load_dword v4, v[12:13], off
	global_load_dword v5, v[14:15], off
	global_load_dword v6, v[16:17], off
	global_load_dword v7, v[18:19], off
	global_load_dword v8, v[20:21], off
	global_load_dword v9, v[22:23], off
	global_load_dword v10, v[24:25], off
	s_movk_i32 s2, 0x200
	v_cmp_gt_u32_e64 s[2:3], s2, v0
	s_and_saveexec_b64 s[4:5], s[2:3]
	s_cbranch_execz .LBB4_2
	s_mov_b64 s[6:7], s[16:17]
	global_load_dword v11, v2, s[6:7]
.LBB4_2:
	s_or_b64 exec, exec, s[4:5]
	v_cmp_gt_u32_e64 s[4:5], 16, v0
	v_mov_b32_e32 v12, 0
	v_mov_b32_e32 v13, 0
	v_mov_b32_e32 v14, 0
	v_mov_b32_e32 v15, 0
	v_mov_b32_e32 v16, 0
	v_mov_b32_e32 v17, 0
	v_mov_b32_e32 v18, 0
	s_and_saveexec_b64 s[6:7], s[4:5]
	s_cbranch_execz .LBB4_4
	s_mov_b64 s[8:9], s[14:15]
	v_lshlrev_b32_e32 v20, 6, v0
	v_mov_b32_e32 v21, 0
	s_waitcnt lgkmcnt(0)
	v_lshl_add_u64 v[12:13], s[8:9], 0, v[20:21]
	v_add_co_u32_e32 v22, vcc, 0x1000, v12
	s_nop 1
	v_addc_co_u32_e32 v23, vcc, 0, v13, vcc
	global_load_dword v3, v20, s[8:9]
	global_load_dword v12, v20, s[8:9] offset:1024
	global_load_dword v13, v20, s[8:9] offset:2048
	global_load_dword v14, v20, s[8:9] offset:3072
	global_load_dword v15, v[22:23], off
	global_load_dword v16, v[22:23], off offset:1024
	global_load_dword v17, v[22:23], off offset:2048
	global_load_dword v18, v[22:23], off offset:3072
.LBB4_4:
	s_or_b64 exec, exec, s[6:7]
	v_and_b32_e32 v19, 7, v0
	v_lshlrev_b32_e32 v19, 2, v19
	global_load_dword v38, v19, s[18:19]
	s_waitcnt vmcnt(7)
	v_add_f32_e32 v1, 0, v1
	s_waitcnt vmcnt(6)
	v_add_f32_e32 v1, v1, v4
	s_waitcnt vmcnt(5)
	v_add_f32_e32 v1, v1, v5
	s_waitcnt vmcnt(4)
	v_add_f32_e32 v1, v1, v6
	s_waitcnt vmcnt(3)
	v_add_f32_e32 v1, v1, v7
	s_waitcnt vmcnt(2)
	v_add_f32_e32 v1, v1, v8
	s_waitcnt vmcnt(1)
	v_add_f32_e32 v1, v1, v9
	s_waitcnt vmcnt(0)
	v_add_f32_e32 v1, v1, v10
	ds_write_b32 v2, v1
	s_and_saveexec_b64 s[6:7], s[2:3]
	ds_write_b32 v2, v11 offset:4096
	s_or_b64 exec, exec, s[6:7]
	s_and_saveexec_b64 s[2:3], s[4:5]
	v_add_u32_e32 v1, v12, v3
	v_add3_u32 v1, v13, v1, v14
	v_add3_u32 v1, v15, v1, v16
	v_add3_u32 v1, v17, v1, v18
	ds_write_b32 v2, v1 offset:6144
	s_or_b64 exec, exec, s[2:3]
	s_movk_i32 s2, 0x80
	v_cmp_gt_u32_e32 vcc, s2, v0
	s_waitcnt lgkmcnt(0)
	s_barrier
	s_and_saveexec_b64 s[2:3], vcc
	s_cbranch_execz .LBB4_12
	v_lshrrev_b32_e32 v3, 3, v0
	v_lshlrev_b32_e32 v1, 2, v3
	ds_read_b32 v1, v1 offset:6144
	s_mov_b64 s[4:5], s[18:19]
	s_mov_b64 s[6:7], s[20:21]
	v_and_b32_e32 v0, 7, v0
	v_mov_b32_e32 v5, 0x1000
	v_lshlrev_b32_e32 v3, 8, v3
	s_waitcnt lgkmcnt(0)
	v_cvt_f32_i32_e32 v4, v1
	v_mov_b32_e32 v1, 0
	v_max_f32_e32 v6, 1.0, v4
	v_div_scale_f32 v7, s[0:1], v6, v6, 1.0
	v_rcp_f32_e32 v8, v7
	v_lshl_or_b32 v4, v0, 8, v5
	v_div_scale_f32 v5, vcc, 1.0, v6, 1.0
	v_fma_f32 v9, -v7, v8, 1.0
	v_fmac_f32_e32 v8, v9, v8
	v_mul_f32_e32 v9, v5, v8
	v_fma_f32 v10, -v7, v9, v5
	v_fmac_f32_e32 v9, v10, v8
	v_fma_f32 v5, -v7, v9, v5
	v_div_fmas_f32 v5, v5, v8, v9
	v_div_fixup_f32 v5, v5, v6, 1.0
	s_mov_b32 s0, 0
.LBB4_10:
	v_add_u32_e32 v18, s0, v3
	v_add_u32_e32 v34, s0, v4
	ds_read_b128 v[6:9], v18
	ds_read_b128 v[10:13], v18 offset:16
	ds_read_b128 v[14:17], v18 offset:32
	ds_read_b128 v[18:21], v18 offset:48
	ds_read_b128 v[22:25], v34
	ds_read_b128 v[26:29], v34 offset:16
	ds_read_b128 v[30:33], v34 offset:32
	ds_read_b128 v[34:37], v34 offset:48
	s_waitcnt lgkmcnt(7)
	v_mul_f32_e32 v6, v5, v6
	v_mul_f32_e32 v7, v5, v7
	s_waitcnt lgkmcnt(3)
	v_fmac_f32_e32 v1, v6, v22
	v_mul_f32_e32 v8, v5, v8
	v_fmac_f32_e32 v1, v7, v23
	v_mul_f32_e32 v9, v5, v9
	v_fmac_f32_e32 v1, v8, v24
	v_mul_f32_e32 v10, v5, v10
	v_fmac_f32_e32 v1, v9, v25
	v_mul_f32_e32 v11, v5, v11
	s_waitcnt lgkmcnt(2)
	v_fmac_f32_e32 v1, v10, v26
	v_mul_f32_e32 v12, v5, v12
	v_fmac_f32_e32 v1, v11, v27
	v_mul_f32_e32 v13, v5, v13
	v_fmac_f32_e32 v1, v12, v28
	v_mul_f32_e32 v14, v5, v14
	v_fmac_f32_e32 v1, v13, v29
	v_mul_f32_e32 v15, v5, v15
	s_waitcnt lgkmcnt(1)
	v_fmac_f32_e32 v1, v14, v30
	v_mul_f32_e32 v16, v5, v16
	v_fmac_f32_e32 v1, v15, v31
	v_mul_f32_e32 v17, v5, v17
	v_fmac_f32_e32 v1, v16, v32
	v_mul_f32_e32 v18, v5, v18
	v_fmac_f32_e32 v1, v17, v33
	v_mul_f32_e32 v19, v5, v19
	s_waitcnt lgkmcnt(0)
	v_fmac_f32_e32 v1, v18, v34
	v_mul_f32_e32 v20, v5, v20
	v_fmac_f32_e32 v1, v19, v35
	s_add_i32 s0, s0, 64
	v_mul_f32_e32 v21, v5, v21
	v_fmac_f32_e32 v1, v20, v36
	s_cmpk_eq_i32 s0, 0x100
	v_fmac_f32_e32 v1, v21, v37
	s_cbranch_scc0 .LBB4_10
	v_add_f32_e32 v0, v1, v38
	global_store_dword v2, v0, s[6:7]

	.amdhsa_kernel _Z7k_finalPKfPKiS0_S0_Pf
		.amdhsa_group_segment_fixed_size 6208
		.amdhsa_private_segment_fixed_size 0
		.amdhsa_kernarg_size 40
		.amdhsa_user_sgpr_count 2
		.amdhsa_user_sgpr_dispatch_ptr 0
		.amdhsa_user_sgpr_queue_ptr 0
		.amdhsa_user_sgpr_kernarg_segment_ptr 1
		.amdhsa_user_sgpr_dispatch_id 0
		.amdhsa_user_sgpr_kernarg_preload_length 0
		.amdhsa_user_sgpr_kernarg_preload_offset 0
		.amdhsa_user_sgpr_private_segment_size 0
		.amdhsa_uses_dynamic_stack 0
		.amdhsa_enable_private_segment 0
		.amdhsa_system_sgpr_workgroup_id_x 1
		.amdhsa_system_sgpr_workgroup_id_y 0
		.amdhsa_system_sgpr_workgroup_id_z 0
		.amdhsa_system_sgpr_workgroup_info 0
		.amdhsa_system_vgpr_workitem_id 0
		.amdhsa_next_free_vgpr 40
		.amdhsa_next_free_sgpr 24
		.amdhsa_accum_offset 40
		.amdhsa_reserve_vcc 1
		.amdhsa_float_round_mode_32 0
		.amdhsa_float_round_mode_16_64 0
		.amdhsa_float_denorm_mode_32 3
		.amdhsa_float_denorm_mode_16_64 3
		.amdhsa_dx10_clamp 1
		.amdhsa_ieee_mode 1
		.amdhsa_fp16_overflow 0
		.amdhsa_tg_split 0
		.amdhsa_exception_fp_ieee_invalid_op 0
		.amdhsa_exception_fp_denorm_src 0
		.amdhsa_exception_fp_ieee_div_zero 0
		.amdhsa_exception_fp_ieee_overflow 0
		.amdhsa_exception_fp_ieee_underflow 0
		.amdhsa_exception_fp_ieee_inexact 0
		.amdhsa_exception_int_div_zero 0
	.end_amdhsa_kernel

amdhsa.kernels:
  - .agpr_count:     0
    .args:
      - .actual_access:  read_only
        .address_space:  global
        .offset:         0
        .size:           8
        .value_kind:     global_buffer
      - .actual_access:  read_only
        .address_space:  global
        .offset:         8
        .size:           8
        .value_kind:     global_buffer
      - .actual_access:  read_only
        .address_space:  global
        .offset:         16
        .size:           8
        .value_kind:     global_buffer
      - .actual_access:  read_only
        .address_space:  global
        .offset:         24
        .size:           8
        .value_kind:     global_buffer
      - .actual_access:  write_only
        .address_space:  global
        .offset:         32
        .size:           8
        .value_kind:     global_buffer
      - .actual_access:  write_only
        .address_space:  global
        .offset:         40
        .size:           8
        .value_kind:     global_buffer
      - .actual_access:  write_only
        .address_space:  global
        .offset:         48
        .size:           8
        .value_kind:     global_buffer
      - .actual_access:  write_only
        .address_space:  global
        .offset:         56
        .size:           8
        .value_kind:     global_buffer
      - .actual_access:  write_only
        .address_space:  global
        .offset:         64
        .size:           8
        .value_kind:     global_buffer
      - .offset:         72
        .size:           4
        .value_kind:     by_value
      - .offset:         80
        .size:           4
        .value_kind:     hidden_block_count_x
      - .offset:         84
        .size:           4
        .value_kind:     hidden_block_count_y
      - .offset:         88
        .size:           4
        .value_kind:     hidden_block_count_z
      - .offset:         92
        .size:           2
        .value_kind:     hidden_group_size_x
      - .offset:         94
        .size:           2
        .value_kind:     hidden_group_size_y
      - .offset:         96
        .size:           2
        .value_kind:     hidden_group_size_z
      - .offset:         98
        .size:           2
        .value_kind:     hidden_remainder_x
      - .offset:         100
        .size:           2
        .value_kind:     hidden_remainder_y
      - .offset:         102
        .size:           2
        .value_kind:     hidden_remainder_z
      - .offset:         120
        .size:           8
        .value_kind:     hidden_global_offset_x
      - .offset:         128
        .size:           8
        .value_kind:     hidden_global_offset_y
      - .offset:         136
        .size:           8
        .value_kind:     hidden_global_offset_z
      - .offset:         144
        .size:           2
        .value_kind:     hidden_grid_dims
    .group_segment_fixed_size: 0
    .kernarg_segment_align: 8
    .kernarg_segment_size: 336
    .language:       OpenCL C
    .language_version:
      - 2
      - 0
    .max_flat_workgroup_size: 256
    .name:           _Z7k_prepwPKfS0_S0_S0_PfPDF16_S2_S2_Pii
    .private_segment_fixed_size: 0
    .sgpr_count:     30
    .sgpr_spill_count: 0
    .symbol:         _Z7k_prepwPKfS0_S0_S0_PfPDF16_S2_S2_Pii.kd
    .uniform_work_group_size: 1
    .uses_dynamic_stack: false
    .vgpr_count:     72
    .vgpr_spill_count: 0
    .wavefront_size: 64
  - .agpr_count:     4
    .args:
      - .actual_access:  read_only
        .address_space:  global
        .offset:         0
        .size:           8
        .value_kind:     global_buffer
      - .actual_access:  read_only
        .address_space:  global
        .offset:         8
        .size:           8
        .value_kind:     global_buffer
      - .address_space:  global
        .offset:         16
        .size:           8
        .value_kind:     global_buffer
      - .actual_access:  write_only
        .address_space:  global
        .offset:         24
        .size:           8
        .value_kind:     global_buffer
      - .address_space:  global
        .offset:         32
        .size:           8
        .value_kind:     global_buffer
      - .address_space:  global
        .offset:         40
        .size:           8
        .value_kind:     global_buffer
      - .actual_access:  write_only
        .address_space:  global
        .offset:         48
        .size:           8
        .value_kind:     global_buffer
      - .actual_access:  write_only
        .address_space:  global
        .offset:         56
        .size:           8
        .value_kind:     global_buffer
      - .actual_access:  write_only
        .address_space:  global
        .offset:         64
        .size:           8
        .value_kind:     global_buffer
      - .actual_access:  read_only
        .address_space:  global
        .offset:         72
        .size:           8
        .value_kind:     global_buffer
      - .actual_access:  read_only
        .address_space:  global
        .offset:         80
        .size:           8
        .value_kind:     global_buffer
      - .actual_access:  write_only
        .address_space:  global
        .offset:         88
        .size:           8
        .value_kind:     global_buffer
      - .actual_access:  write_only
        .address_space:  global
        .offset:         96
        .size:           8
        .value_kind:     global_buffer
    .group_segment_fixed_size: 8200
    .kernarg_segment_align: 8
    .kernarg_segment_size: 104
    .language:       OpenCL C
    .language_version:
      - 2
      - 0
    .max_flat_workgroup_size: 128
    .name:           _Z6k_prepPKiS0_PiS1_S1_S1_S1_S1_S1_PKfPKDF16_PDF16_Pf
    .private_segment_fixed_size: 0
    .sgpr_count:     54
    .sgpr_spill_count: 0
    .symbol:         _Z6k_prepPKiS0_PiS1_S1_S1_S1_S1_S1_PKfPKDF16_PDF16_Pf.kd
    .uniform_work_group_size: 1
    .uses_dynamic_stack: false
    .vgpr_count:     96
    .vgpr_spill_count: 0
    .wavefront_size: 64
  - .agpr_count:     0
    .args:
      - .actual_access:  read_only
        .address_space:  global
        .offset:         0
        .size:           8
        .value_kind:     global_buffer
      - .actual_access:  read_only
        .address_space:  global
        .offset:         8
        .size:           8
        .value_kind:     global_buffer
      - .actual_access:  read_only
        .address_space:  global
        .offset:         16
        .size:           8
        .value_kind:     global_buffer
      - .actual_access:  read_only
        .address_space:  global
        .offset:         24
        .size:           8
        .value_kind:     global_buffer
      - .actual_access:  read_only
        .address_space:  global
        .offset:         32
        .size:           8
        .value_kind:     global_buffer
      - .actual_access:  read_only
        .address_space:  global
        .offset:         40
        .size:           8
        .value_kind:     global_buffer
      - .actual_access:  read_only
        .address_space:  global
        .offset:         48
        .size:           8
        .value_kind:     global_buffer
      - .actual_access:  read_only
        .address_space:  global
        .offset:         56
        .size:           8
        .value_kind:     global_buffer
      - .actual_access:  read_only
        .address_space:  global
        .offset:         64
        .size:           8
        .value_kind:     global_buffer
      - .actual_access:  read_only
        .address_space:  global
        .offset:         72
        .size:           8
        .value_kind:     global_buffer
      - .actual_access:  read_only
        .address_space:  global
        .offset:         80
        .size:           8
        .value_kind:     global_buffer
      - .actual_access:  read_only
        .address_space:  global
        .offset:         88
        .size:           8
        .value_kind:     global_buffer
      - .actual_access:  read_only
        .address_space:  global
        .offset:         96
        .size:           8
        .value_kind:     global_buffer
      - .actual_access:  read_only
        .address_space:  global
        .offset:         104
        .size:           8
        .value_kind:     global_buffer
      - .actual_access:  read_only
        .address_space:  global
        .offset:         112
        .size:           8
        .value_kind:     global_buffer
      - .actual_access:  read_only
        .address_space:  global
        .offset:         120
        .size:           8
        .value_kind:     global_buffer
      - .actual_access:  write_only
        .address_space:  global
        .offset:         128
        .size:           8
        .value_kind:     global_buffer
      - .actual_access:  write_only
        .address_space:  global
        .offset:         136
        .size:           8
        .value_kind:     global_buffer
    .group_segment_fixed_size: 81920
    .kernarg_segment_align: 8
    .kernarg_segment_size: 144
    .language:       OpenCL C
    .language_version:
      - 2
      - 0
    .max_flat_workgroup_size: 512
    .name:           _Z4k_l1PKDF16_PKfPKiS4_S4_S4_S4_S4_S4_S2_S2_S0_S0_S2_S2_S2_PDF16_Pf
    .private_segment_fixed_size: 0
    .sgpr_count:     57
    .sgpr_spill_count: 0
    .symbol:         _Z4k_l1PKDF16_PKfPKiS4_S4_S4_S4_S4_S4_S2_S2_S0_S0_S2_S2_S2_PDF16_Pf.kd
    .uniform_work_group_size: 1
    .uses_dynamic_stack: false
    .vgpr_count:     128
    .vgpr_spill_count: 0
    .wavefront_size: 64
  - .agpr_count:     0
    .args:
      - .actual_access:  read_only
        .address_space:  global
        .offset:         0
        .size:           8
        .value_kind:     global_buffer
      - .actual_access:  read_only
        .address_space:  global
        .offset:         8
        .size:           8
        .value_kind:     global_buffer
      - .actual_access:  read_only
        .address_space:  global
        .offset:         16
        .size:           8
        .value_kind:     global_buffer
      - .actual_access:  read_only
        .address_space:  global
        .offset:         24
        .size:           8
        .value_kind:     global_buffer
      - .actual_access:  read_only
        .address_space:  global
        .offset:         32
        .size:           8
        .value_kind:     global_buffer
      - .actual_access:  read_only
        .address_space:  global
        .offset:         40
        .size:           8
        .value_kind:     global_buffer
      - .actual_access:  read_only
        .address_space:  global
        .offset:         48
        .size:           8
        .value_kind:     global_buffer
      - .actual_access:  read_only
        .address_space:  global
        .offset:         56
        .size:           8
        .value_kind:     global_buffer
      - .actual_access:  read_only
        .address_space:  global
        .offset:         64
        .size:           8
        .value_kind:     global_buffer
      - .actual_access:  read_only
        .address_space:  global
        .offset:         72
        .size:           8
        .value_kind:     global_buffer
      - .actual_access:  read_only
        .address_space:  global
        .offset:         80
        .size:           8
        .value_kind:     global_buffer
      - .actual_access:  read_only
        .address_space:  global
        .offset:         88
        .size:           8
        .value_kind:     global_buffer
      - .address_space:  global
        .offset:         96
        .size:           8
        .value_kind:     global_buffer
      - .address_space:  global
        .offset:         104
        .size:           8
        .value_kind:     global_buffer
      - .offset:         112
        .size:           4
        .value_kind:     hidden_block_count_x
      - .offset:         116
        .size:           4
        .value_kind:     hidden_block_count_y
      - .offset:         120
        .size:           4
        .value_kind:     hidden_block_count_z
      - .offset:         124
        .size:           2
        .value_kind:     hidden_group_size_x
      - .offset:         126
        .size:           2
        .value_kind:     hidden_group_size_y
      - .offset:         128
        .size:           2
        .value_kind:     hidden_group_size_z
      - .offset:         130
        .size:           2
        .value_kind:     hidden_remainder_x
      - .offset:         132
        .size:           2
        .value_kind:     hidden_remainder_y
      - .offset:         134
        .size:           2
        .value_kind:     hidden_remainder_z
      - .offset:         152
        .size:           8
        .value_kind:     hidden_global_offset_x
      - .offset:         160
        .size:           8
        .value_kind:     hidden_global_offset_y
      - .offset:         168
        .size:           8
        .value_kind:     hidden_global_offset_z
      - .offset:         176
        .size:           2
        .value_kind:     hidden_grid_dims
    .group_segment_fixed_size: 4160
    .kernarg_segment_align: 8
    .kernarg_segment_size: 368
    .language:       OpenCL C
    .language_version:
      - 2
      - 0
    .max_flat_workgroup_size: 256
    .name:           _Z4k_l2PKDF16_PKfPKiS4_S4_S4_S4_S4_S4_S2_S2_S2_PfPi
    .private_segment_fixed_size: 0
    .sgpr_count:     54
    .sgpr_spill_count: 0
    .symbol:         _Z4k_l2PKDF16_PKfPKiS4_S4_S4_S4_S4_S4_S2_S2_S2_PfPi.kd
    .uniform_work_group_size: 1
    .uses_dynamic_stack: false
    .vgpr_count:     118
    .vgpr_spill_count: 0
    .wavefront_size: 64
  - .agpr_count:     0
    .args:
      - .actual_access:  read_only
        .address_space:  global
        .offset:         0
        .size:           8
        .value_kind:     global_buffer
      - .actual_access:  read_only
        .address_space:  global
        .offset:         8
        .size:           8
        .value_kind:     global_buffer
      - .actual_access:  read_only
        .address_space:  global
        .offset:         16
        .size:           8
        .value_kind:     global_buffer
      - .actual_access:  read_only
        .address_space:  global
        .offset:         24
        .size:           8
        .value_kind:     global_buffer
      - .actual_access:  write_only
        .address_space:  global
        .offset:         32
        .size:           8
        .value_kind:     global_buffer
    .group_segment_fixed_size: 6208
    .kernarg_segment_align: 8
    .kernarg_segment_size: 40
    .language:       OpenCL C
    .language_version:
      - 2
      - 0
    .max_flat_workgroup_size: 1024
    .name:           _Z7k_finalPKfPKiS0_S0_Pf
    .private_segment_fixed_size: 0
    .sgpr_count:     30
    .sgpr_spill_count: 0
    .symbol:         _Z7k_finalPKfPKiS0_S0_Pf.kd
    .uniform_work_group_size: 1
    .uses_dynamic_stack: false
    .vgpr_count:     40
    .vgpr_spill_count: 0
    .wavefront_size: 64
